# v096 k-snake + P0 rmsnorm prefetch + P3 K-loop in the same order (shifted-tuple groups kept as plain chains)
# speedup vs baseline: 1.0140x; 1.0057x over previous
.LBB0_563:
	v_add_u32_e32 v3, 0x10000, v209
	ds_read_b128 v[140:143], v3
	ds_read_b128 v[144:147], v3 offset:1024
	ds_read_b128 v[148:151], v3 offset:2048
	ds_read_b128 v[152:155], v3 offset:3072
	v_add_u32_e32 v3, 0x14000, v209
	ds_read_b128 v[156:159], v3
	ds_read_b128 v[160:163], v3 offset:1024
	ds_read_b128 v[164:167], v3 offset:2048
	ds_read_b128 v[168:171], v3 offset:3072
	s_add_i32 s10, s57, 0xfff80080
	s_cmp_eq_u32 s59, 12
	s_cselect_b32 s62, s2, s10
	s_cselect_b32 s61, s3, s58
	s_add_i32 s60, s62, 0x80
	s_mov_b32 m0, s44
	ds_read_b128 v[172:175], v210
	ds_read_b128 v[176:179], v210 offset:1024
	ds_read_b128 v[180:183], v210 offset:2048
	ds_read_b128 v[184:187], v210 offset:3072
	ds_read_b128 v[188:191], v210 offset:4096
	ds_read_b128 v[192:195], v210 offset:5120
	ds_read_b128 v[196:199], v210 offset:6144
	ds_read_b128 v[200:203], v210 offset:7168
	buffer_load_dwordx4 v1, s[4:7], s57 offen lds
	s_mov_b32 m0, s45
	s_nop 0
	buffer_load_dwordx4 v206, s[4:7], s57 offen lds
	s_waitcnt vmcnt(8)
	s_waitcnt lgkmcnt(0)
	s_barrier
	s_waitcnt lgkmcnt(7)
	v_mfma_f32_16x16x32_bf16 v[130:133], v[140:143], v[172:175], v[130:133]
	v_mfma_f32_16x16x32_bf16 v[130:133], v[144:147], v[176:179], v[130:133]
	s_waitcnt lgkmcnt(5)
	v_mfma_f32_16x16x32_bf16 v[126:129], v[152:155], v[176:179], v[126:129]
	v_mfma_f32_16x16x32_bf16 v[126:129], v[148:151], v[172:175], v[126:129]
	s_waitcnt lgkmcnt(3)
	v_mfma_f32_16x16x32_bf16 v[118:121], v[148:151], v[180:183], v[118:121]
	v_mfma_f32_16x16x32_bf16 v[118:121], v[152:155], v[184:187], v[118:121]
	s_waitcnt lgkmcnt(1)
	v_mfma_f32_16x16x32_bf16 v[122:125], v[144:147], v[184:187], v[122:125]
	v_mfma_f32_16x16x32_bf16 v[122:125], v[140:143], v[180:183], v[122:125]
	v_mfma_f32_16x16x32_bf16 v[114:117], v[140:143], v[188:191], v[114:117]
	v_mfma_f32_16x16x32_bf16 v[114:117], v[144:147], v[192:195], v[114:117]
	v_mfma_f32_16x16x32_bf16 v[110:113], v[152:155], v[192:195], v[110:113]
	v_mfma_f32_16x16x32_bf16 v[110:113], v[148:151], v[188:191], v[110:113]
	v_mfma_f32_16x16x32_bf16 v[102:105], v[148:151], v[196:199], v[102:105]
	v_mfma_f32_16x16x32_bf16 v[102:105], v[152:155], v[200:203], v[102:105]
	s_waitcnt lgkmcnt(0)
	v_mfma_f32_16x16x32_bf16 v[106:109], v[144:147], v[200:203], v[106:109]
	v_mfma_f32_16x16x32_bf16 v[106:109], v[140:143], v[196:199], v[106:109]
	v_mfma_f32_16x16x32_bf16 v[98:101], v[156:159], v[172:175], v[98:101]
	v_mfma_f32_16x16x32_bf16 v[98:101], v[160:163], v[176:179], v[98:101]
	v_mfma_f32_16x16x32_bf16 v[94:97], v[168:171], v[176:179], v[94:97]
	v_mfma_f32_16x16x32_bf16 v[94:97], v[164:167], v[172:175], v[94:97]
	v_mfma_f32_16x16x32_bf16 v[86:89], v[164:167], v[180:183], v[86:89]
	v_mfma_f32_16x16x32_bf16 v[86:89], v[168:171], v[184:187], v[86:89]
	v_mfma_f32_16x16x32_bf16 v[90:93], v[160:163], v[184:187], v[90:93]
	v_mfma_f32_16x16x32_bf16 v[90:93], v[156:159], v[180:183], v[90:93]
	v_mfma_f32_16x16x32_bf16 v[82:85], v[156:159], v[188:191], v[82:85]
	v_mfma_f32_16x16x32_bf16 v[82:85], v[160:163], v[192:195], v[82:85]
	v_mfma_f32_16x16x32_bf16 v[78:81], v[168:171], v[192:195], v[78:81]
	v_mfma_f32_16x16x32_bf16 v[78:81], v[164:167], v[188:191], v[78:81]
	v_mfma_f32_16x16x32_bf16 v[70:73], v[164:167], v[196:199], v[70:73]
	v_mfma_f32_16x16x32_bf16 v[70:73], v[168:171], v[200:203], v[70:73]
	v_mfma_f32_16x16x32_bf16 v[74:77], v[160:163], v[200:203], v[74:77]
	v_mfma_f32_16x16x32_bf16 v[74:77], v[156:159], v[196:199], v[74:77]
	s_barrier
	s_mov_b32 m0, s28
	s_mov_b32 s10, s6
	s_mov_b32 s11, s7
	ds_read_b128 v[172:175], v210 offset:16384
	ds_read_b128 v[176:179], v210 offset:17408
	ds_read_b128 v[180:183], v210 offset:18432
	ds_read_b128 v[184:187], v210 offset:19456
	ds_read_b128 v[188:191], v210 offset:20480
	ds_read_b128 v[192:195], v210 offset:21504
	ds_read_b128 v[196:199], v210 offset:22528
	ds_read_b128 v[200:203], v210 offset:23552
	buffer_load_dwordx4 v135, s[8:11], s61 offen lds
	s_mov_b32 m0, s29
	s_add_i32 s63, s61, 0x80000
	buffer_load_dwordx4 v207, s[8:11], s61 offen lds
	s_mov_b32 m0, s30
	s_nop 0
	buffer_load_dwordx4 v135, s[8:11], s63 offen lds
	s_mov_b32 m0, s31
	s_nop 0
	buffer_load_dwordx4 v207, s[8:11], s63 offen lds
	s_mov_b32 m0, s27
	s_nop 0
	buffer_load_dwordx4 v1, s[4:7], s62 offen lds
	s_mov_b32 m0, s33
	s_nop 0
	buffer_load_dwordx4 v206, s[4:7], s62 offen lds
	s_waitcnt vmcnt(8)
	s_waitcnt lgkmcnt(0)
	s_barrier
	s_waitcnt lgkmcnt(7)
	v_mfma_f32_16x16x32_bf16 v[66:69], v[140:143], v[172:175], v[66:69]
	v_mfma_f32_16x16x32_bf16 v[66:69], v[144:147], v[176:179], v[66:69]
	s_waitcnt lgkmcnt(5)
	v_mfma_f32_16x16x32_bf16 v[62:65], v[152:155], v[176:179], v[62:65]
	v_mfma_f32_16x16x32_bf16 v[62:65], v[148:151], v[172:175], v[62:65]
	s_waitcnt lgkmcnt(3)
	v_mfma_f32_16x16x32_bf16 v[54:57], v[148:151], v[180:183], v[54:57]
	v_mfma_f32_16x16x32_bf16 v[54:57], v[152:155], v[184:187], v[54:57]
	s_waitcnt lgkmcnt(1)
	v_mfma_f32_16x16x32_bf16 v[58:61], v[144:147], v[184:187], v[58:61]
	v_mfma_f32_16x16x32_bf16 v[58:61], v[140:143], v[180:183], v[58:61]
	v_mfma_f32_16x16x32_bf16 v[50:53], v[140:143], v[188:191], v[50:53]
	v_mfma_f32_16x16x32_bf16 v[50:53], v[144:147], v[192:195], v[50:53]
	v_mfma_f32_16x16x32_bf16 v[46:49], v[152:155], v[192:195], v[46:49]
	v_mfma_f32_16x16x32_bf16 v[46:49], v[148:151], v[188:191], v[46:49]
	v_mfma_f32_16x16x32_bf16 v[38:41], v[148:151], v[196:199], v[38:41]
	v_mfma_f32_16x16x32_bf16 v[38:41], v[152:155], v[200:203], v[38:41]
	s_waitcnt lgkmcnt(0)
	v_mfma_f32_16x16x32_bf16 v[42:45], v[144:147], v[200:203], v[42:45]
	v_mfma_f32_16x16x32_bf16 v[42:45], v[140:143], v[196:199], v[42:45]
	v_mfma_f32_16x16x32_bf16 v[34:37], v[156:159], v[172:175], v[34:37]
	v_mfma_f32_16x16x32_bf16 v[34:37], v[160:163], v[176:179], v[34:37]
	v_mfma_f32_16x16x32_bf16 v[30:33], v[164:167], v[172:175], v[30:33]
	v_mfma_f32_16x16x32_bf16 v[30:33], v[168:171], v[176:179], v[30:33]
	v_mfma_f32_16x16x32_bf16 v[26:29], v[156:159], v[180:183], v[26:29]
	v_mfma_f32_16x16x32_bf16 v[26:29], v[160:163], v[184:187], v[26:29]
	v_mfma_f32_16x16x32_bf16 v[22:25], v[164:167], v[180:183], v[22:25]
	v_mfma_f32_16x16x32_bf16 v[22:25], v[168:171], v[184:187], v[22:25]
	v_mfma_f32_16x16x32_bf16 v[18:21], v[156:159], v[188:191], v[18:21]
	v_mfma_f32_16x16x32_bf16 v[18:21], v[160:163], v[192:195], v[18:21]
	v_mfma_f32_16x16x32_bf16 v[14:17], v[164:167], v[188:191], v[14:17]
	v_mfma_f32_16x16x32_bf16 v[14:17], v[168:171], v[192:195], v[14:17]
	v_mfma_f32_16x16x32_bf16 v[10:13], v[156:159], v[196:199], v[10:13]
	v_mfma_f32_16x16x32_bf16 v[10:13], v[160:163], v[200:203], v[10:13]
	v_mfma_f32_16x16x32_bf16 v[4:7], v[164:167], v[196:199], v[6:9]
	v_mfma_f32_16x16x32_bf16 v[4:7], v[168:171], v[200:203], v[4:7]
	s_barrier
	v_add_u32_e32 v3, 0x18000, v209
	ds_read_b128 v[140:143], v3
	ds_read_b128 v[144:147], v3 offset:1024
	ds_read_b128 v[148:151], v3 offset:2048
	ds_read_b128 v[152:155], v3 offset:3072
	v_add_u32_e32 v3, 0x1c000, v209
	ds_read_b128 v[156:159], v3
	ds_read_b128 v[160:163], v3 offset:1024
	ds_read_b128 v[164:167], v3 offset:2048
	ds_read_b128 v[168:171], v3 offset:3072
	s_add_i32 s62, s62, 0x80000
	s_mov_b32 m0, s34
	ds_read_b128 v[172:175], v210 offset:32768
	ds_read_b128 v[176:179], v210 offset:33792
	ds_read_b128 v[180:183], v210 offset:34816
	ds_read_b128 v[184:187], v210 offset:35840
	ds_read_b128 v[188:191], v210 offset:36864
	ds_read_b128 v[192:195], v210 offset:37888
	ds_read_b128 v[196:199], v210 offset:38912
	ds_read_b128 v[200:203], v210 offset:39936
	buffer_load_dwordx4 v1, s[4:7], s62 offen lds
	s_mov_b32 m0, s35
	s_nop 0
	buffer_load_dwordx4 v206, s[4:7], s62 offen lds
	s_waitcnt vmcnt(8)
	s_waitcnt lgkmcnt(0)
	s_barrier
	s_waitcnt lgkmcnt(7)
	v_mfma_f32_16x16x32_bf16 v[130:133], v[140:143], v[172:175], v[130:133]
	v_mfma_f32_16x16x32_bf16 v[130:133], v[144:147], v[176:179], v[130:133]
	s_waitcnt lgkmcnt(5)
	v_mfma_f32_16x16x32_bf16 v[126:129], v[152:155], v[176:179], v[126:129]
	v_mfma_f32_16x16x32_bf16 v[126:129], v[148:151], v[172:175], v[126:129]
	s_waitcnt lgkmcnt(3)
	v_mfma_f32_16x16x32_bf16 v[118:121], v[148:151], v[180:183], v[118:121]
	v_mfma_f32_16x16x32_bf16 v[118:121], v[152:155], v[184:187], v[118:121]
	s_waitcnt lgkmcnt(1)
	v_mfma_f32_16x16x32_bf16 v[122:125], v[144:147], v[184:187], v[122:125]
	v_mfma_f32_16x16x32_bf16 v[122:125], v[140:143], v[180:183], v[122:125]
	v_mfma_f32_16x16x32_bf16 v[114:117], v[140:143], v[188:191], v[114:117]
	v_mfma_f32_16x16x32_bf16 v[114:117], v[144:147], v[192:195], v[114:117]
	v_mfma_f32_16x16x32_bf16 v[110:113], v[152:155], v[192:195], v[110:113]
	v_mfma_f32_16x16x32_bf16 v[110:113], v[148:151], v[188:191], v[110:113]
	v_mfma_f32_16x16x32_bf16 v[102:105], v[148:151], v[196:199], v[102:105]
	v_mfma_f32_16x16x32_bf16 v[102:105], v[152:155], v[200:203], v[102:105]
	s_waitcnt lgkmcnt(0)
	v_mfma_f32_16x16x32_bf16 v[106:109], v[144:147], v[200:203], v[106:109]
	v_mfma_f32_16x16x32_bf16 v[106:109], v[140:143], v[196:199], v[106:109]
	v_mfma_f32_16x16x32_bf16 v[98:101], v[156:159], v[172:175], v[98:101]
	v_mfma_f32_16x16x32_bf16 v[98:101], v[160:163], v[176:179], v[98:101]
	v_mfma_f32_16x16x32_bf16 v[94:97], v[168:171], v[176:179], v[94:97]
	v_mfma_f32_16x16x32_bf16 v[94:97], v[164:167], v[172:175], v[94:97]
	v_mfma_f32_16x16x32_bf16 v[86:89], v[164:167], v[180:183], v[86:89]
	v_mfma_f32_16x16x32_bf16 v[86:89], v[168:171], v[184:187], v[86:89]
	v_mfma_f32_16x16x32_bf16 v[90:93], v[160:163], v[184:187], v[90:93]
	v_mfma_f32_16x16x32_bf16 v[90:93], v[156:159], v[180:183], v[90:93]
	v_mfma_f32_16x16x32_bf16 v[82:85], v[156:159], v[188:191], v[82:85]
	v_mfma_f32_16x16x32_bf16 v[82:85], v[160:163], v[192:195], v[82:85]
	v_mfma_f32_16x16x32_bf16 v[78:81], v[168:171], v[192:195], v[78:81]
	v_mfma_f32_16x16x32_bf16 v[78:81], v[164:167], v[188:191], v[78:81]
	v_mfma_f32_16x16x32_bf16 v[70:73], v[164:167], v[196:199], v[70:73]
	v_mfma_f32_16x16x32_bf16 v[70:73], v[168:171], v[200:203], v[70:73]
	v_mfma_f32_16x16x32_bf16 v[74:77], v[160:163], v[200:203], v[74:77]
	v_mfma_f32_16x16x32_bf16 v[74:77], v[156:159], v[196:199], v[74:77]
	s_barrier
	s_mov_b32 m0, s38
	s_add_i32 s62, s61, 0x80
	ds_read_b128 v[172:175], v210 offset:49152
	ds_read_b128 v[176:179], v210 offset:50176
	ds_read_b128 v[180:183], v210 offset:51200
	ds_read_b128 v[184:187], v210 offset:52224
	ds_read_b128 v[188:191], v210 offset:53248
	ds_read_b128 v[192:195], v210 offset:54272
	ds_read_b128 v[196:199], v210 offset:55296
	ds_read_b128 v[200:203], v210 offset:56320
	buffer_load_dwordx4 v135, s[8:11], s62 offen lds
	s_mov_b32 m0, s39
	s_add_i32 s61, s61, 0x80080
	buffer_load_dwordx4 v207, s[8:11], s62 offen lds
	s_mov_b32 m0, s42
	s_nop 0
	buffer_load_dwordx4 v135, s[8:11], s61 offen lds
	s_mov_b32 m0, s43
	s_nop 0
	buffer_load_dwordx4 v207, s[8:11], s61 offen lds
	s_mov_b32 m0, s40
	s_nop 0
	buffer_load_dwordx4 v1, s[4:7], s60 offen lds
	s_mov_b32 m0, s41
	s_nop 0
	buffer_load_dwordx4 v206, s[4:7], s60 offen lds
	s_waitcnt vmcnt(8)
	s_waitcnt lgkmcnt(0)
	s_barrier
	s_waitcnt lgkmcnt(7)
	v_mfma_f32_16x16x32_bf16 v[66:69], v[140:143], v[172:175], v[66:69]
	v_mfma_f32_16x16x32_bf16 v[66:69], v[144:147], v[176:179], v[66:69]
	s_waitcnt lgkmcnt(5)
	v_mfma_f32_16x16x32_bf16 v[62:65], v[152:155], v[176:179], v[62:65]
	v_mfma_f32_16x16x32_bf16 v[62:65], v[148:151], v[172:175], v[62:65]
	s_waitcnt lgkmcnt(3)
	v_mfma_f32_16x16x32_bf16 v[54:57], v[148:151], v[180:183], v[54:57]
	v_mfma_f32_16x16x32_bf16 v[54:57], v[152:155], v[184:187], v[54:57]
	s_waitcnt lgkmcnt(1)
	v_mfma_f32_16x16x32_bf16 v[58:61], v[144:147], v[184:187], v[58:61]
	v_mfma_f32_16x16x32_bf16 v[58:61], v[140:143], v[180:183], v[58:61]
	v_mfma_f32_16x16x32_bf16 v[50:53], v[140:143], v[188:191], v[50:53]
	v_mfma_f32_16x16x32_bf16 v[50:53], v[144:147], v[192:195], v[50:53]
	v_mfma_f32_16x16x32_bf16 v[46:49], v[152:155], v[192:195], v[46:49]
	v_mfma_f32_16x16x32_bf16 v[46:49], v[148:151], v[188:191], v[46:49]
	v_mfma_f32_16x16x32_bf16 v[38:41], v[148:151], v[196:199], v[38:41]
	v_mfma_f32_16x16x32_bf16 v[38:41], v[152:155], v[200:203], v[38:41]
	s_waitcnt lgkmcnt(0)
	v_mfma_f32_16x16x32_bf16 v[42:45], v[144:147], v[200:203], v[42:45]
	v_mfma_f32_16x16x32_bf16 v[42:45], v[140:143], v[196:199], v[42:45]
	v_mfma_f32_16x16x32_bf16 v[34:37], v[156:159], v[172:175], v[34:37]
	v_mfma_f32_16x16x32_bf16 v[34:37], v[160:163], v[176:179], v[34:37]
	v_mfma_f32_16x16x32_bf16 v[30:33], v[164:167], v[172:175], v[30:33]
	v_mfma_f32_16x16x32_bf16 v[30:33], v[168:171], v[176:179], v[30:33]
	v_mfma_f32_16x16x32_bf16 v[26:29], v[156:159], v[180:183], v[26:29]
	v_mfma_f32_16x16x32_bf16 v[26:29], v[160:163], v[184:187], v[26:29]
	v_mfma_f32_16x16x32_bf16 v[22:25], v[164:167], v[180:183], v[22:25]
	v_mfma_f32_16x16x32_bf16 v[22:25], v[168:171], v[184:187], v[22:25]
	v_mfma_f32_16x16x32_bf16 v[18:21], v[156:159], v[188:191], v[18:21]
	v_mfma_f32_16x16x32_bf16 v[18:21], v[160:163], v[192:195], v[18:21]
	v_mfma_f32_16x16x32_bf16 v[14:17], v[164:167], v[188:191], v[14:17]
	v_mfma_f32_16x16x32_bf16 v[14:17], v[168:171], v[192:195], v[14:17]
	v_mfma_f32_16x16x32_bf16 v[8:11], v[156:159], v[196:199], v[10:13]
	v_mfma_f32_16x16x32_bf16 v[10:13], v[160:163], v[200:203], v[8:11]
	v_mfma_f32_16x16x32_bf16 v[4:7], v[164:167], v[196:199], v[4:7]
	v_mfma_f32_16x16x32_bf16 v[6:9], v[168:171], v[200:203], v[4:7]
	s_barrier
	s_add_i32 s59, s59, 2
	s_addk_i32 s57, 0x100
	s_addk_i32 s58, 0x100
	s_cmp_gt_u32 s59, 13
	s_cbranch_scc0 .LBB0_563
	s_and_b64 vcc, exec, s[20:21]
	s_cbranch_vccz .LBB0_566
	s_barrier
